# grid barrier: the completing leader no longer waits for the acknowledgement of its generation add before leaving the barrier
# speedup vs baseline: 1.0032x; 1.0008x over previous
; __device__ __forceinline__ unsigned xb_ld(unsigned* p)              { return __hip_atomic_load(p, __ATOMIC_RELAXED, __HIP_MEMORY_SCOPE_AGENT); }
; __device__ __forceinline__ unsigned xb_add(unsigned* p, unsigned v) { return __hip_atomic_fetch_add(p, v, __ATOMIC_RELAXED, __HIP_MEMORY_SCOPE_AGENT); }
; #define XB_SPIN(cond, bar) do { unsigned _sp = 0; while (cond) { __builtin_amdgcn_s_sleep(1); \
;     if ((++_sp & 255u) == 0u) { if (xb_ld(&(bar)[XB_TMO])) break; if (_sp > XB_SPIN_CAP) { atomicAdd(&(bar)[XB_TMO], 1u); break; } } } } while (0)
; __device__ __forceinline__ void xcd_barrier(const XcdBarrier& b) {
;     ...
;             __builtin_amdgcn_fence(__ATOMIC_ACQUIRE, "agent");
;             xb_add(&bar[XB_XGEN(b.x)], 1u);
;             asm volatile("s_waitcnt vmcnt(0)" ::: "memory");
;         } else {
;             XB_SPIN(xb_ld(&bar[XB_XGEN(b.x)]) == gen, bar);
;             __builtin_amdgcn_fence(__ATOMIC_ACQUIRE, "agent");
;             asm volatile("s_waitcnt vmcnt(0)" ::: "memory");
;         }
;     }
;     __syncthreads();
.LBB0_190:
	s_or_b64 exec, exec, s[0:1]
	v_readlane_b32 s0, v247, 57
	v_readlane_b32 s1, v247, 58
	s_nop 2
